# v13 + ml_a unit: wave-0 gate load/scan moved behind the issue of the unit's k/v loads (one round trip instead of two)
# speedup vs baseline: 1.0050x; 1.0013x over previous
.LBB0_609:
	s_mul_hi_i32 s14, s24, 0x38e38e39
	s_lshr_b32 s15, s14, 31
	s_ashr_i32 s14, s14, 3
	s_add_i32 s14, s14, s15
	s_mul_i32 s15, s14, 36
	s_sub_i32 s15, s24, s15
	s_ashr_i32 s43, s14, 3
	s_bfe_u32 s44, s14, 0x20001
	s_and_b32 s16, s14, 1
	s_mov_b32 s98, s16
	s_cmp_lt_i32 s15, 4
	s_cselect_b32 s14, 32, -4
	s_add_i32 s25, s14, s15
	s_sub_i32 s42, 35, s15
	s_cmp_eq_u32 s16, 0
	s_cselect_b64 s[14:15], -1, 0
	s_and_b64 s[28:29], s[14:15], exec
	s_cselect_b32 s25, s25, s42
	s_and_b64 vcc, exec, s[12:13]
	s_lshl_b32 s42, s25, 6
.LBB0_617:
	s_lshl_b32 s14, s43, 8
	s_addk_i32 s14, 0x1800
	s_lshl_b32 s15, s43, 11
	v_or_b32_e32 v4, s42, v14
	v_cmp_gt_i32_e32 vcc, s39, v4
	v_mov_b32_e32 v8, s14
	v_mov_b32_e32 v12, s15
	s_lshl_b32 s16, s44, 8
	v_cndmask_b32_e32 v5, v8, v12, vcc
	v_lshl_add_u64 v[2:3], v[10:11], 0, s[16:17]
	v_add_u32_e32 v4, v5, v4
	v_mad_i64_i32 v[4:5], s[14:15], v4, s40, v[2:3]
	global_load_ushort v13, v[4:5], off offset:2048
	global_load_ushort v62, v[4:5], off offset:1024
	v_or_b32_e32 v4, s42, v15
	v_cmp_gt_i32_e32 vcc, s39, v4
	s_nop 1
	v_cndmask_b32_e32 v5, v8, v12, vcc
	v_add_u32_e32 v4, v5, v4
	v_mad_i64_i32 v[4:5], s[14:15], v4, s40, v[2:3]
	global_load_ushort v63, v[4:5], off offset:2048
	global_load_ushort v64, v[4:5], off offset:1024
	v_or_b32_e32 v4, s42, v28
	v_cmp_gt_i32_e32 vcc, s39, v4
	s_nop 1
	v_cndmask_b32_e32 v5, v8, v12, vcc
	v_add_u32_e32 v4, v5, v4
	v_mad_i64_i32 v[4:5], s[14:15], v4, s40, v[2:3]
	global_load_ushort v65, v[4:5], off offset:2048
	global_load_ushort v66, v[4:5], off offset:1024
	v_or_b32_e32 v4, s42, v16
	v_cmp_gt_i32_e32 vcc, s39, v4
	s_nop 1
	v_cndmask_b32_e32 v5, v8, v12, vcc
	v_add_u32_e32 v4, v5, v4
	v_mad_i64_i32 v[4:5], s[14:15], v4, s40, v[2:3]
	global_load_ushort v67, v[4:5], off offset:2048
	global_load_ushort v68, v[4:5], off offset:1024
	v_or_b32_e32 v4, s42, v30
	v_cmp_gt_i32_e32 vcc, s39, v4
	s_nop 1
	v_cndmask_b32_e32 v5, v8, v12, vcc
	v_add_u32_e32 v4, v5, v4
	v_mad_i64_i32 v[4:5], s[14:15], v4, s40, v[2:3]
	global_load_ushort v69, v[4:5], off offset:2048
	global_load_ushort v70, v[4:5], off offset:1024
	v_or_b32_e32 v4, s42, v17
	v_cmp_gt_i32_e32 vcc, s39, v4
	s_nop 1
	v_cndmask_b32_e32 v5, v8, v12, vcc
	v_add_u32_e32 v4, v5, v4
	v_mad_i64_i32 v[4:5], s[14:15], v4, s40, v[2:3]
	global_load_ushort v71, v[4:5], off offset:2048
	global_load_ushort v72, v[4:5], off offset:1024
	v_or_b32_e32 v4, s42, v32
	v_cmp_gt_i32_e32 vcc, s39, v4
	s_nop 1
	v_cndmask_b32_e32 v5, v8, v12, vcc
	v_add_u32_e32 v4, v5, v4
	v_mad_i64_i32 v[4:5], s[14:15], v4, s40, v[2:3]
	global_load_ushort v73, v[4:5], off offset:2048
	global_load_ushort v74, v[4:5], off offset:1024
	v_or_b32_e32 v4, s42, v18
	v_cmp_gt_i32_e32 vcc, s39, v4
	s_nop 1
	v_cndmask_b32_e32 v5, v8, v12, vcc
	v_add_u32_e32 v4, v5, v4
	v_mad_i64_i32 v[4:5], s[14:15], v4, s40, v[2:3]
	global_load_ushort v75, v[4:5], off offset:2048
	global_load_ushort v76, v[4:5], off offset:1024
	v_or_b32_e32 v4, s42, v34
	v_cmp_gt_i32_e32 vcc, s39, v4
	s_nop 1
	v_cndmask_b32_e32 v5, v8, v12, vcc
	v_add_u32_e32 v4, v5, v4
	v_mad_i64_i32 v[4:5], s[14:15], v4, s40, v[2:3]
	global_load_ushort v77, v[4:5], off offset:2048
	global_load_ushort v78, v[4:5], off offset:1024
	v_or_b32_e32 v4, s42, v19
	v_cmp_gt_i32_e32 vcc, s39, v4
	s_nop 1
	v_cndmask_b32_e32 v5, v8, v12, vcc
	v_add_u32_e32 v4, v5, v4
	v_mad_i64_i32 v[4:5], s[14:15], v4, s40, v[2:3]
	global_load_ushort v79, v[4:5], off offset:2048
	global_load_ushort v80, v[4:5], off offset:1024
	v_or_b32_e32 v4, s42, v36
	v_cmp_gt_i32_e32 vcc, s39, v4
	s_nop 1
	v_cndmask_b32_e32 v5, v8, v12, vcc
	v_add_u32_e32 v4, v5, v4
	v_mad_i64_i32 v[4:5], s[14:15], v4, s40, v[2:3]
	global_load_ushort v81, v[4:5], off offset:2048
	global_load_ushort v82, v[4:5], off offset:1024
	v_or_b32_e32 v4, s42, v20
	v_cmp_gt_i32_e32 vcc, s39, v4
	s_nop 1
	v_cndmask_b32_e32 v5, v8, v12, vcc
	v_add_u32_e32 v4, v5, v4
	v_mad_i64_i32 v[4:5], s[14:15], v4, s40, v[2:3]
	global_load_ushort v83, v[4:5], off offset:2048
	global_load_ushort v84, v[4:5], off offset:1024
	v_or_b32_e32 v4, s42, v38
	v_cmp_gt_i32_e32 vcc, s39, v4
	s_nop 1
	v_cndmask_b32_e32 v5, v8, v12, vcc
	v_add_u32_e32 v4, v5, v4
	v_mad_i64_i32 v[4:5], s[14:15], v4, s40, v[2:3]
	global_load_ushort v85, v[4:5], off offset:2048
	global_load_ushort v86, v[4:5], off offset:1024
	v_or_b32_e32 v4, s42, v21
	v_cmp_gt_i32_e32 vcc, s39, v4
	s_nop 1
	v_cndmask_b32_e32 v5, v8, v12, vcc
	v_add_u32_e32 v4, v5, v4
	v_mad_i64_i32 v[4:5], s[14:15], v4, s40, v[2:3]
	global_load_ushort v87, v[4:5], off offset:2048
	global_load_ushort v88, v[4:5], off offset:1024
	v_or_b32_e32 v4, s42, v39
	v_cmp_gt_i32_e32 vcc, s39, v4
	s_nop 1
	v_cndmask_b32_e32 v5, v8, v12, vcc
	v_add_u32_e32 v4, v5, v4
	v_mad_i64_i32 v[4:5], s[14:15], v4, s40, v[2:3]
	global_load_ushort v89, v[4:5], off offset:2048
	global_load_ushort v90, v[4:5], off offset:1024
	v_add_u32_e32 v4, s42, v22
	v_cmp_gt_i32_e32 vcc, s39, v4
	s_nop 1
	v_cndmask_b32_e32 v5, v8, v12, vcc
	v_add_u32_e32 v4, v5, v4
	v_mad_i64_i32 v[2:3], s[14:15], v4, s40, v[2:3]
	global_load_ushort v4, v[2:3], off offset:2048
	s_nop 0
	global_load_ushort v2, v[2:3], off offset:1024
	s_and_b64 vcc, exec, s[12:13]
	s_cbranch_vccnz .Lmla_skip_0
	s_cmp_eq_u32 s98, 0
	s_cselect_b64 s[14:15], -1, 0
	v_or_b32_e32 v249, s42, v164
	s_movk_i32 s25, 0x7ff
	v_cmp_lt_i32_e32 vcc, s25, v249
	s_and_saveexec_b64 s[28:29], vcc
	s_xor_b64 s[28:29], exec, s[28:29]
	s_lshl_b32 s25, s43, 8
	s_addk_i32 s25, 0x1800
	v_add_u32_e32 v248, s25, v249
	s_andn2_saveexec_b64 s[28:29], s[28:29]
	v_lshl_add_u32 v248, s43, 11, v249
	s_or_b64 exec, exec, s[28:29]
	v_ashrrev_i32_e32 v249, 31, v248
	v_lshlrev_b64 v[248:249], 6, v[248:249]
	s_lshl_b32 s25, s44, 2
	s_lshl_b32 s16, s98, 4
	v_lshl_add_u64 v[248:249], s[18:19], 0, v[248:249]
	s_or_b32 s16, s16, s25
	v_lshl_add_u64 v[248:249], v[248:249], 0, s[16:17]
	global_load_dword v250, v[248:249], off
	s_nop 0
	global_load_dword v248, v[248:249], off offset:32
	s_waitcnt vmcnt(0)
	s_nop 0
	v_add_f32_dpp v249, v248, v248 row_shr:1 row_mask:0xf bank_mask:0xf bound_ctrl:1
	s_nop 1
	v_add_f32_dpp v249, v249, v249 row_shr:2 row_mask:0xf bank_mask:0xf bound_ctrl:1
	s_nop 1
	v_add_f32_dpp v249, v249, v249 row_shr:4 row_mask:0xf bank_mask:0xf bound_ctrl:1
	s_nop 1
	v_add_f32_dpp v249, v249, v249 row_shr:8 row_mask:0xf bank_mask:0xf bound_ctrl:1
	s_nop 0
	v_readlane_b32 s16, v249, 15
	v_readlane_b32 s25, v249, 31
	v_readlane_b32 s28, v249, 47
	v_mov_b32_e32 v251, s16
	v_cndmask_b32_e64 v251, 0, v251, s[0:1]
	v_add_f32_e32 v249, v249, v251
	v_mov_b32_e32 v251, s25
	v_cndmask_b32_e64 v251, 0, v251, s[4:5]
	v_add_f32_e32 v249, v249, v251
	v_mov_b32_e32 v251, s28
	v_cndmask_b32_e64 v251, 0, v251, s[6:7]
	v_add_f32_e32 v249, v249, v251
	v_sub_f32_e32 v248, v249, v248
	v_readlane_b32 s16, v249, 63
	s_nop 1
	v_sub_f32_e32 v251, s16, v249
	v_cndmask_b32_e64 v248, v248, v251, s[14:15]
	v_add_f32_e32 v248, v250, v248
	s_nop 1
	v_mov_b32_dpp v249, v248 quad_perm:[1,0,3,2] row_mask:0xf bank_mask:0xf bound_ctrl:1
	v_max_f32_e32 v249, v249, v249
	v_max_f32_e32 v249, v248, v249
	s_nop 1
	v_mov_b32_dpp v250, v249 quad_perm:[2,3,0,1] row_mask:0xf bank_mask:0xf bound_ctrl:1
	v_max_f32_e32 v250, v250, v250
	v_max_f32_e32 v249, v249, v250
	s_nop 1
	v_mov_b32_dpp v250, v249 row_half_mirror row_mask:0xf bank_mask:0xf bound_ctrl:1
	v_max_f32_e32 v250, v250, v250
	v_max_f32_e32 v249, v249, v250
	s_nop 1
	v_mov_b32_dpp v250, v249 row_mirror row_mask:0xf bank_mask:0xf bound_ctrl:1
	v_max_f32_e32 v250, v250, v250
	v_max_f32_e32 v249, v249, v250
	s_nop 0
	v_readlane_b32 s25, v249, 32
	v_readlane_b32 s28, v249, 48
	v_readlane_b32 s14, v249, 0
	v_readlane_b32 s15, v249, 16
	v_max_f32_e64 v249, s28, s28
	v_max_f32_e64 v250, s25, s25
	v_max_f32_e32 v249, v250, v249
	v_mov_b32_e32 v250, s15
	v_max3_f32 v249, s14, v250, v249
	v_sub_f32_e32 v248, v248, v249
	v_mul_f32_e32 v248, 0x3fb8aa3b, v248
	v_exp_f32_e32 v248, v248
	ds_write_b32 v27, v248 offset:39168
	s_and_saveexec_b64 s[14:15], s[8:9]
	s_cbranch_execz .LBB0_616
	s_ashr_i32 s25, s24, 31
	s_lshl_b64 s[28:29], s[24:25], 4
	s_add_u32 s28, s34, s28
	s_addc_u32 s29, s35, s29
	v_mov_b32_e32 v248, s16
	global_store_dwordx2 v9, v[248:249], s[28:29]

.Lmla_skip_0:
	s_waitcnt vmcnt(17)
	s_nop 0
	v_lshlrev_b32_e32 v12, 16, v63
	v_lshlrev_b32_e32 v63, 16, v67
	v_lshlrev_b32_e32 v67, 16, v71
	v_lshlrev_b32_e32 v71, 16, v75
	s_waitcnt vmcnt(1)
	s_nop 0
	v_lshlrev_b32_e32 v75, 16, v79
	v_lshlrev_b32_e32 v79, 16, v83
	v_lshlrev_b32_e32 v83, 16, v87
	v_add_u32_e32 v87, 0x9800, v40
	s_waitcnt vmcnt(0)
	v_lshlrev_b32_e32 v3, 16, v4
	s_waitcnt lgkmcnt(0)
	s_barrier
	ds_read2_b32 v[4:5], v87 offset0:64 offset1:72
	v_lshlrev_b32_e32 v8, 16, v13
	v_lshlrev_b32_e32 v13, 16, v65
	v_lshlrev_b32_e32 v65, 16, v69
	v_lshlrev_b32_e32 v69, 16, v73
	s_waitcnt lgkmcnt(0)
	v_mul_f32_e32 v4, v4, v8
	v_cvt_pk_bf16_f32 v4, v4, v9
	ds_write_b16 v41, v4
	ds_write_b16 v41, v62 offset:20736
	ds_read_b32 v4, v42 offset:39168
	v_lshlrev_b32_e32 v73, 16, v77
	v_lshlrev_b32_e32 v77, 16, v81
	v_lshlrev_b32_e32 v81, 16, v85
	v_lshlrev_b32_e32 v85, 16, v89
	s_waitcnt lgkmcnt(0)
	v_mul_f32_e32 v4, v4, v12
	v_cvt_pk_bf16_f32 v4, v4, v9
	ds_write_b16 v43, v4
	ds_write_b16 v43, v64 offset:20736
	v_mul_f32_e32 v4, v5, v13
	v_cvt_pk_bf16_f32 v4, v4, v9
	ds_write_b16 v41, v4 offset:16
	ds_write_b16 v41, v66 offset:20752
	ds_read_b32 v4, v44 offset:39168
	s_mov_b64 s[14:15], 0
	s_waitcnt lgkmcnt(0)
	v_mul_f32_e32 v4, v4, v63
	v_cvt_pk_bf16_f32 v4, v4, v9
	ds_write_b16 v45, v4
	ds_write_b16 v45, v68 offset:20736
	ds_read2_b32 v[4:5], v87 offset0:80 offset1:88
	s_waitcnt lgkmcnt(0)
	v_mul_f32_e32 v4, v4, v65
	v_cvt_pk_bf16_f32 v4, v4, v9
	ds_write_b16 v41, v4 offset:32
	ds_write_b16 v41, v70 offset:20768
	ds_read_b32 v4, v46 offset:39168
	s_waitcnt lgkmcnt(0)
	v_mul_f32_e32 v4, v4, v67
	v_cvt_pk_bf16_f32 v4, v4, v9
	ds_write_b16 v47, v4
	ds_write_b16 v47, v72 offset:20736
	v_mul_f32_e32 v4, v5, v69
	v_cvt_pk_bf16_f32 v4, v4, v9
	ds_write_b16 v41, v4 offset:48
	ds_write_b16 v41, v74 offset:20784
	ds_read_b32 v4, v48 offset:39168
	s_waitcnt lgkmcnt(0)
	v_mul_f32_e32 v4, v4, v71
	v_cvt_pk_bf16_f32 v4, v4, v9
	ds_write_b16 v49, v4
	ds_write_b16 v49, v76 offset:20736
	ds_read2_b32 v[4:5], v87 offset0:96 offset1:104
	s_waitcnt lgkmcnt(0)
	v_mul_f32_e32 v4, v4, v73
	v_cvt_pk_bf16_f32 v4, v4, v9
	ds_write_b16 v41, v4 offset:64
	ds_write_b16 v41, v78 offset:20800
	ds_read_b32 v4, v50 offset:39168
	s_waitcnt lgkmcnt(0)
	v_mul_f32_e32 v4, v4, v75
	v_cvt_pk_bf16_f32 v4, v4, v9
	ds_write_b16 v51, v4
	ds_write_b16 v51, v80 offset:20736
	v_mul_f32_e32 v4, v5, v77
	v_cvt_pk_bf16_f32 v4, v4, v9
	ds_write_b16 v41, v4 offset:80
	ds_write_b16 v41, v82 offset:20816
	ds_read_b32 v4, v52 offset:39168
	s_waitcnt lgkmcnt(0)
	v_mul_f32_e32 v4, v4, v79
	v_cvt_pk_bf16_f32 v4, v4, v9
	ds_write_b16 v53, v4
	ds_write_b16 v53, v84 offset:20736
	ds_read2_b32 v[4:5], v87 offset0:112 offset1:120
	s_waitcnt lgkmcnt(0)
	v_mul_f32_e32 v4, v4, v81
	v_cvt_pk_bf16_f32 v4, v4, v9
	ds_write_b16 v41, v4 offset:96
	ds_write_b16 v41, v86 offset:20832
	ds_read_b32 v4, v54 offset:39168
	s_waitcnt lgkmcnt(0)
	v_mul_f32_e32 v4, v4, v83
	v_cvt_pk_bf16_f32 v4, v4, v9
	ds_write_b16 v55, v4
	ds_write_b16 v55, v88 offset:20736
	v_mul_f32_e32 v4, v5, v85
	v_cvt_pk_bf16_f32 v4, v4, v9
	ds_write_b16 v41, v4 offset:112
	ds_write_b16 v41, v90 offset:20848
	ds_read_b32 v4, v56 offset:39168
	s_waitcnt lgkmcnt(0)
	v_mul_f32_e32 v3, v4, v3
	v_cvt_pk_bf16_f32 v3, v3, v9
	ds_write_b16 v57, v3
	ds_write_b16 v57, v2 offset:20736
	v_mov_b32_e32 v2, v58
	v_mov_b32_e32 v3, v0
	s_branch .LBB0_619

.LBB0_2792:
	s_mul_hi_i32 s14, s24, 0x38e38e39
	s_lshr_b32 s15, s14, 31
	s_ashr_i32 s14, s14, 3
	s_add_i32 s14, s14, s15
	s_mul_i32 s15, s14, 36
	s_sub_i32 s15, s24, s15
	s_ashr_i32 s44, s14, 3
	s_bfe_u32 s45, s14, 0x20001
	s_and_b32 s16, s14, 1
	s_mov_b32 s98, s16
	s_cmp_lt_i32 s15, 4
	s_cselect_b32 s14, 32, -4
	s_add_i32 s25, s14, s15
	s_sub_i32 s43, 35, s15
	s_cmp_eq_u32 s16, 0
	s_cselect_b64 s[14:15], -1, 0
	s_and_b64 s[28:29], s[14:15], exec
	s_cselect_b32 s25, s25, s43
	s_and_b64 vcc, exec, s[12:13]
	s_lshl_b32 s43, s25, 6
.LBB0_2800:
	s_lshl_b32 s14, s44, 8
	s_addk_i32 s14, 0x1800
	s_lshl_b32 s15, s44, 11
	v_or_b32_e32 v4, s43, v14
	v_mov_b32_e32 v6, s14
	v_mov_b32_e32 v66, s15
	v_cmp_gt_i32_e32 vcc, s39, v4
	v_or_b32_e32 v12, s43, v15
	v_or_b32_e32 v62, s43, v28
	v_cndmask_b32_e32 v5, v6, v66, vcc
	v_cmp_gt_i32_e32 vcc, s39, v12
	v_or_b32_e32 v64, s43, v16
	s_lshl_b32 s16, s45, 8
	v_cndmask_b32_e32 v13, v6, v66, vcc
	v_cmp_gt_i32_e32 vcc, s39, v62
	v_lshl_add_u64 v[2:3], v[10:11], 0, s[16:17]
	v_add_u32_e32 v4, v5, v4
	v_cndmask_b32_e32 v63, v6, v66, vcc
	v_cmp_gt_i32_e32 vcc, s39, v64
	v_mad_i64_i32 v[4:5], s[14:15], v4, s40, v[2:3]
	s_nop 0
	v_cndmask_b32_e32 v65, v6, v66, vcc
	v_add_u32_e32 v12, v13, v12
	v_add_u32_e32 v62, v63, v62
	v_add_u32_e32 v64, v65, v64
	v_mad_i64_i32 v[12:13], s[14:15], v12, s40, v[2:3]
	v_mad_i64_i32 v[62:63], s[14:15], v62, s40, v[2:3]
	v_mad_i64_i32 v[64:65], s[14:15], v64, s40, v[2:3]
	global_load_ushort v67, v[4:5], off offset:2048
	global_load_ushort v68, v[12:13], off offset:2048
	global_load_ushort v69, v[62:63], off offset:2048
	global_load_ushort v70, v[64:65], off offset:2048
	global_load_ushort v71, v[64:65], off offset:1024
	global_load_ushort v72, v[62:63], off offset:1024
	global_load_ushort v73, v[12:13], off offset:1024
	global_load_ushort v74, v[4:5], off offset:1024
	v_or_b32_e32 v4, s43, v30
	v_cmp_gt_i32_e32 vcc, s39, v4
	v_or_b32_e32 v12, s43, v17
	v_or_b32_e32 v62, s43, v32
	v_cndmask_b32_e32 v5, v6, v66, vcc
	v_cmp_gt_i32_e32 vcc, s39, v12
	v_or_b32_e32 v64, s43, v18
	v_add_u32_e32 v4, v5, v4
	v_cndmask_b32_e32 v13, v6, v66, vcc
	v_cmp_gt_i32_e32 vcc, s39, v62
	v_mad_i64_i32 v[4:5], s[14:15], v4, s40, v[2:3]
	s_nop 0
	v_cndmask_b32_e32 v63, v6, v66, vcc
	v_cmp_gt_i32_e32 vcc, s39, v64
	v_add_u32_e32 v12, v13, v12
	v_add_u32_e32 v62, v63, v62
	v_cndmask_b32_e32 v65, v6, v66, vcc
	v_add_u32_e32 v64, v65, v64
	v_mad_i64_i32 v[12:13], s[14:15], v12, s40, v[2:3]
	v_mad_i64_i32 v[62:63], s[14:15], v62, s40, v[2:3]
	v_mad_i64_i32 v[64:65], s[14:15], v64, s40, v[2:3]
	global_load_ushort v75, v[4:5], off offset:2048
	global_load_ushort v76, v[12:13], off offset:2048
	global_load_ushort v77, v[62:63], off offset:2048
	global_load_ushort v78, v[64:65], off offset:2048
	global_load_ushort v79, v[64:65], off offset:1024
	global_load_ushort v80, v[62:63], off offset:1024
	global_load_ushort v81, v[12:13], off offset:1024
	global_load_ushort v82, v[4:5], off offset:1024
	v_or_b32_e32 v4, s43, v34
	v_cmp_gt_i32_e32 vcc, s39, v4
	v_or_b32_e32 v12, s43, v19
	v_or_b32_e32 v62, s43, v36
	v_cndmask_b32_e32 v5, v6, v66, vcc
	v_cmp_gt_i32_e32 vcc, s39, v12
	v_or_b32_e32 v64, s43, v20
	v_add_u32_e32 v4, v5, v4
	v_cndmask_b32_e32 v13, v6, v66, vcc
	v_cmp_gt_i32_e32 vcc, s39, v62
	v_mad_i64_i32 v[4:5], s[14:15], v4, s40, v[2:3]
	s_nop 0
	v_cndmask_b32_e32 v63, v6, v66, vcc
	v_cmp_gt_i32_e32 vcc, s39, v64
	v_add_u32_e32 v12, v13, v12
	v_add_u32_e32 v62, v63, v62
	v_cndmask_b32_e32 v65, v6, v66, vcc
	v_add_u32_e32 v64, v65, v64
	v_mad_i64_i32 v[64:65], s[14:15], v64, s40, v[2:3]
	v_mad_i64_i32 v[12:13], s[14:15], v12, s40, v[2:3]
	v_mad_i64_i32 v[62:63], s[14:15], v62, s40, v[2:3]
	global_load_ushort v83, v[4:5], off offset:2048
	global_load_ushort v84, v[12:13], off offset:2048
	global_load_ushort v85, v[62:63], off offset:2048
	global_load_ushort v86, v[64:65], off offset:2048
	s_nop 0
	global_load_ushort v64, v[64:65], off offset:1024
	s_nop 0
	global_load_ushort v65, v[62:63], off offset:1024
	global_load_ushort v87, v[12:13], off offset:1024
	global_load_ushort v88, v[4:5], off offset:1024
	v_or_b32_e32 v4, s43, v38
	v_cmp_gt_i32_e32 vcc, s39, v4
	v_or_b32_e32 v12, s43, v21
	v_or_b32_e32 v62, s43, v39
	v_cndmask_b32_e32 v5, v6, v66, vcc
	v_cmp_gt_i32_e32 vcc, s39, v12
	v_add_u32_e32 v89, s43, v22
	v_add_u32_e32 v4, v5, v4
	v_cndmask_b32_e32 v13, v6, v66, vcc
	v_cmp_gt_i32_e32 vcc, s39, v62
	v_add_u32_e32 v12, v13, v12
	v_mad_i64_i32 v[4:5], s[14:15], v4, s40, v[2:3]
	v_cndmask_b32_e32 v63, v6, v66, vcc
	v_cmp_gt_i32_e32 vcc, s39, v89
	v_add_u32_e32 v62, v63, v62
	v_mad_i64_i32 v[12:13], s[14:15], v12, s40, v[2:3]
	v_cndmask_b32_e32 v6, v6, v66, vcc
	v_mad_i64_i32 v[62:63], s[14:15], v62, s40, v[2:3]
	v_add_u32_e32 v6, v6, v89
	v_mad_i64_i32 v[2:3], s[14:15], v6, s40, v[2:3]
	global_load_ushort v6, v[4:5], off offset:2048
	global_load_ushort v66, v[12:13], off offset:2048
	global_load_ushort v89, v[62:63], off offset:2048
	global_load_ushort v90, v[2:3], off offset:2048
	global_load_ushort v91, v[2:3], off offset:1024
	s_nop 0
	global_load_ushort v62, v[62:63], off offset:1024
	s_nop 0
	global_load_ushort v12, v[12:13], off offset:1024
	s_nop 0
	global_load_ushort v4, v[4:5], off offset:1024
	s_and_b64 vcc, exec, s[12:13]
	s_cbranch_vccnz .Lmla_skip_1
	s_cmp_eq_u32 s98, 0
	s_cselect_b64 s[14:15], -1, 0
	v_or_b32_e32 v249, s43, v164
	s_movk_i32 s25, 0x7ff
	v_cmp_lt_i32_e32 vcc, s25, v249
	s_and_saveexec_b64 s[28:29], vcc
	s_xor_b64 s[28:29], exec, s[28:29]
	s_lshl_b32 s25, s44, 8
	s_addk_i32 s25, 0x1800
	v_add_u32_e32 v248, s25, v249
	s_andn2_saveexec_b64 s[28:29], s[28:29]
	v_lshl_add_u32 v248, s44, 11, v249
	s_or_b64 exec, exec, s[28:29]
	v_ashrrev_i32_e32 v249, 31, v248
	v_lshlrev_b64 v[248:249], 6, v[248:249]
	s_lshl_b32 s25, s45, 2
	s_lshl_b32 s16, s98, 4
	v_lshl_add_u64 v[248:249], s[18:19], 0, v[248:249]
	s_or_b32 s16, s16, s25
	v_lshl_add_u64 v[248:249], v[248:249], 0, s[16:17]
	global_load_dword v250, v[248:249], off offset:32
	s_nop 0
	global_load_dword v248, v[248:249], off
	s_waitcnt vmcnt(1)
	v_add_f32_dpp v249, v250, v250 row_shr:1 row_mask:0xf bank_mask:0xf bound_ctrl:1
	s_nop 1
	v_add_f32_dpp v249, v249, v249 row_shr:2 row_mask:0xf bank_mask:0xf bound_ctrl:1
	s_nop 1
	v_add_f32_dpp v249, v249, v249 row_shr:4 row_mask:0xf bank_mask:0xf bound_ctrl:1
	s_nop 1
	v_add_f32_dpp v249, v249, v249 row_shr:8 row_mask:0xf bank_mask:0xf bound_ctrl:1
	s_nop 0
	v_readlane_b32 s16, v249, 15
	v_readlane_b32 s25, v249, 31
	v_readlane_b32 s28, v249, 47
	v_mov_b32_e32 v251, s16
	v_mov_b32_e32 v252, s25
	v_cndmask_b32_e64 v251, 0, v251, s[0:1]
	v_mov_b32_e32 v253, s28
	v_cndmask_b32_e64 v252, 0, v252, s[4:5]
	v_add_f32_e32 v249, v249, v251
	v_cndmask_b32_e64 v253, 0, v253, s[6:7]
	v_add_f32_e32 v249, v249, v252
	v_add_f32_e32 v249, v249, v253
	v_sub_f32_e32 v250, v249, v250
	v_readlane_b32 s16, v249, 63
	s_nop 1
	v_sub_f32_e32 v249, s16, v249
	v_cndmask_b32_e64 v249, v250, v249, s[14:15]
	s_waitcnt vmcnt(0)
	v_add_f32_e32 v248, v248, v249
	s_nop 1
	v_mov_b32_dpp v249, v248 quad_perm:[1,0,3,2] row_mask:0xf bank_mask:0xf bound_ctrl:1
	v_max_f32_e32 v249, v249, v249
	v_max_f32_e32 v249, v248, v249
	s_nop 1
	v_mov_b32_dpp v250, v249 quad_perm:[2,3,0,1] row_mask:0xf bank_mask:0xf bound_ctrl:1
	v_max_f32_e32 v250, v250, v250
	v_max_f32_e32 v249, v249, v250
	s_nop 1
	v_mov_b32_dpp v250, v249 row_half_mirror row_mask:0xf bank_mask:0xf bound_ctrl:1
	v_max_f32_e32 v250, v250, v250
	v_max_f32_e32 v249, v249, v250
	s_nop 1
	v_mov_b32_dpp v250, v249 row_mirror row_mask:0xf bank_mask:0xf bound_ctrl:1
	v_max_f32_e32 v250, v250, v250
	v_max_f32_e32 v249, v249, v250
	s_nop 0
	v_readlane_b32 s25, v249, 32
	v_readlane_b32 s28, v249, 48
	v_readlane_b32 s14, v249, 0
	v_readlane_b32 s15, v249, 16
	v_max_f32_e64 v249, s28, s28
	v_max_f32_e64 v250, s25, s25
	v_max_f32_e32 v249, v250, v249
	v_mov_b32_e32 v250, s15
	v_max3_f32 v249, s14, v250, v249
	v_sub_f32_e32 v248, v248, v249
	v_mul_f32_e32 v248, 0x3fb8aa3b, v248
	v_exp_f32_e32 v248, v248
	ds_write_b32 v27, v248 offset:39168
	s_and_saveexec_b64 s[14:15], s[8:9]
	s_cbranch_execz .LBB0_2799
	s_ashr_i32 s25, s24, 31
	s_lshl_b64 s[28:29], s[24:25], 4
	s_add_u32 s28, s34, s28
	s_addc_u32 s29, s35, s29
	v_mov_b32_e32 v248, s16
	global_store_dwordx2 v7, v[248:249], s[28:29]

.Lmla_skip_1:
	s_waitcnt vmcnt(20)
	s_waitcnt vmcnt(4)
	v_lshlrev_b32_e32 v5, 16, v67
	v_lshlrev_b32_e32 v67, 16, v70
	v_lshlrev_b32_e32 v70, 16, v77
	v_lshlrev_b32_e32 v77, 16, v84
	v_add_u32_e32 v84, 0x9800, v40
	s_waitcnt vmcnt(0)
	s_waitcnt lgkmcnt(0)
	s_barrier
	ds_read2_b32 v[2:3], v84 offset0:64 offset1:72
	v_lshlrev_b32_e32 v13, 16, v68
	v_lshlrev_b32_e32 v63, 16, v69
	v_lshlrev_b32_e32 v68, 16, v75
	v_lshlrev_b32_e32 v69, 16, v76
	s_waitcnt lgkmcnt(0)
	v_mul_f32_e32 v2, v2, v5
	v_cvt_pk_bf16_f32 v2, v2, v7
	ds_write_b16 v41, v2
	ds_write_b16 v41, v74 offset:20736
	v_lshlrev_b32_e32 v75, 16, v78
	v_lshlrev_b32_e32 v76, 16, v83
	v_lshlrev_b32_e32 v78, 16, v85
	v_lshlrev_b32_e32 v83, 16, v86
	v_lshlrev_b32_e32 v85, 16, v89
	v_lshlrev_b32_e32 v86, 16, v90
	ds_read_b32 v2, v42 offset:39168
	ds_read_b32 v5, v44 offset:39168
	ds_read_b32 v74, v46 offset:39168
	ds_read_b32 v89, v48 offset:39168
	ds_read_b32 v90, v50 offset:39168
	ds_read_b32 v92, v52 offset:39168
	ds_read_b32 v93, v54 offset:39168
	ds_read_b32 v94, v56 offset:39168
	s_waitcnt lgkmcnt(7)
	v_mul_f32_e32 v2, v2, v13
	v_cvt_pk_bf16_f32 v2, v2, v7
	ds_write_b16 v43, v2
	ds_write_b16 v43, v73 offset:20736
	v_mul_f32_e32 v2, v3, v63
	v_cvt_pk_bf16_f32 v2, v2, v7
	ds_write_b16 v41, v2 offset:16
	ds_write_b16 v41, v72 offset:20752
	ds_read2_b32 v[2:3], v84 offset0:80 offset1:88
	s_waitcnt lgkmcnt(11)
	v_mul_f32_e32 v5, v5, v67
	v_cvt_pk_bf16_f32 v5, v5, v7
	ds_write_b16 v45, v5
	ds_write_b16 v45, v71 offset:20736
	s_waitcnt lgkmcnt(11)
	v_mul_f32_e32 v5, v89, v75
	s_waitcnt lgkmcnt(2)
	v_mul_f32_e32 v2, v2, v68
	v_cvt_pk_bf16_f32 v2, v2, v7
	ds_write_b16 v41, v2 offset:32
	ds_write_b16 v41, v82 offset:20768
	v_mul_f32_e32 v2, v74, v69
	v_cvt_pk_bf16_f32 v2, v2, v7
	ds_write_b16 v47, v2
	ds_write_b16 v47, v81 offset:20736
	v_mul_f32_e32 v2, v3, v70
	v_cvt_pk_bf16_f32 v2, v2, v7
	ds_write_b16 v41, v2 offset:48
	ds_write_b16 v41, v80 offset:20784
	ds_read2_b32 v[2:3], v84 offset0:96 offset1:104
	v_cvt_pk_bf16_f32 v5, v5, v7
	ds_write_b16 v49, v5
	ds_write_b16 v49, v79 offset:20736
	v_lshlrev_b32_e32 v6, 16, v6
	v_mul_f32_e32 v5, v92, v83
	s_waitcnt lgkmcnt(2)
	v_mul_f32_e32 v2, v2, v76
	v_cvt_pk_bf16_f32 v2, v2, v7
	ds_write_b16 v41, v2 offset:64
	ds_write_b16 v41, v88 offset:20800
	v_mul_f32_e32 v2, v90, v77
	v_cvt_pk_bf16_f32 v2, v2, v7
	ds_write_b16 v51, v2
	ds_write_b16 v51, v87 offset:20736
	v_mul_f32_e32 v2, v3, v78
	v_cvt_pk_bf16_f32 v2, v2, v7
	ds_write_b16 v41, v2 offset:80
	ds_write_b16 v41, v65 offset:20816
	ds_read2_b32 v[2:3], v84 offset0:112 offset1:120
	v_lshlrev_b32_e32 v66, 16, v66
	v_cvt_pk_bf16_f32 v5, v5, v7
	ds_write_b16 v53, v5
	ds_write_b16 v53, v64 offset:20736
	s_mov_b64 s[14:15], 0
	s_waitcnt lgkmcnt(2)
	v_mul_f32_e32 v2, v2, v6
	v_cvt_pk_bf16_f32 v2, v2, v7
	ds_write_b16 v41, v2 offset:96
	ds_write_b16 v41, v4 offset:20832
	v_mul_f32_e32 v2, v93, v66
	v_cvt_pk_bf16_f32 v2, v2, v7
	ds_write_b16 v55, v2
	ds_write_b16 v55, v12 offset:20736
	v_mul_f32_e32 v2, v3, v85
	v_cvt_pk_bf16_f32 v2, v2, v7
	ds_write_b16 v41, v2 offset:112
	ds_write_b16 v41, v62 offset:20848
	v_mul_f32_e32 v2, v94, v86
	v_cvt_pk_bf16_f32 v2, v2, v7
	ds_write_b16 v57, v2
	ds_write_b16 v57, v91 offset:20736
	v_mov_b32_e32 v2, v58
	v_mov_b32_e32 v3, v0
	s_branch .LBB0_2802
